# baseline (speedup 1.0000x reference)
.LBB0_78:
	s_load_dwordx8 s[8:15], s[0:1], 0x0
	s_load_dwordx2 s[0:1], s[0:1], 0x28
	v_lshlrev_b32_e32 v2, 9, v0
	v_and_b32_e32 v13, 3, v0
	v_and_b32_e32 v2, 0x7800, v2
	v_mov_b32_e32 v3, 0
	v_lshl_or_b32 v12, s36, 2, v13
	s_waitcnt lgkmcnt(0)
	s_mov_b64 s[44:45], s[0:1]
	v_and_b32_e32 v164, 15, v0
	v_lshlrev_b32_e32 v164, 2, v164
	v_add_u32_e32 v164, 0x14a80, v164
	v_mov_b32_e32 v165, 0
	ds_write_b32 v164, v165
	s_lshl_b32 s46, s33, 8
	v_add_u32_e32 v164, s46, v0
	v_lshrrev_b32_e32 v165, 2, v164
	v_min_u32_e32 v165, 0xc7, v165
	s_mul_i32 s46, s3, 0xc8
	v_add_lshl_u32 v165, v165, s46, 2
	global_load_dword v166, v165, s[8:9]
	global_load_dword v167, v165, s[10:11]
	v_lshl_add_u64 v[4:5], s[0:1], 0, v[2:3]
	s_lshl_b32 s0, s33, 7
	v_lshl_or_b32 v2, v12, 3, s0
	v_lshl_add_u64 v[10:11], v[4:5], 0, v[2:3]
	v_and_b32_e32 v160, 15, v0
	v_bfe_u32 v161, v0, 4, 2
	s_and_b32 s46, s36, 1
	s_lshl_b32 s46, s46, 5
	v_lshl_add_u32 v162, v161, 3, s46
	v_lshlrev_b32_e32 v162, 7, v162
	s_lshl_b32 s47, s33, 5
	s_lshr_b32 s46, s36, 1
	s_add_i32 s47, s47, s46
	v_lshl_add_u32 v163, v160, 1, s47
	v_add_lshl_u32 v162, v162, v163, 2
	global_load_dword v152, v162, s[44:45]
	global_load_dword v153, v162, s[44:45] offset:512
	global_load_dword v154, v162, s[44:45] offset:1024
	global_load_dword v155, v162, s[44:45] offset:1536
	global_load_dword v156, v162, s[44:45] offset:2048
	global_load_dword v157, v162, s[44:45] offset:2560
	global_load_dword v158, v162, s[44:45] offset:3072
	global_load_dword v159, v162, s[44:45] offset:3584
	s_bfe_u32 s5, s2, 0x30002
	s_mov_b32 s4, 2
	s_cmp_gt_u32 s5, 3
	v_lshlrev_b32_e32 v10, 2, v0
	s_cbranch_scc0 .LBB0_80
	v_and_b32_e32 v11, 16, v10
	v_lshl_or_b32 v14, s5, 5, v11
	s_cbranch_execz .LBB0_81
	s_branch .LBB0_82

.Lc_go:
	v_lshrrev_b32_e32 v168, 2, v164
	v_cmp_lt_u32_e32 vcc, 95, v168
	s_and_saveexec_b64 s[48:49], vcc
	v_and_b32_e32 v169, 3, v164
	v_lshlrev_b32_e32 v169, 7, v169
	v_lshl_add_u32 v170, v166, 9, v169
	global_load_dword v171, v170, s[12:13]
	global_load_dword v172, v170, s[12:13] offset:64
	s_movk_i32 s46, 0x2710
	v_mad_u32_u24 v173, v167, s46, v166
	v_lshl_add_u32 v173, v173, 9, v169
	global_load_dword v174, v173, s[14:15]
	global_load_dword v175, v173, s[14:15] offset:64
	s_mov_b64 exec, s[48:49]
	s_cmp_eq_u32 s45, 0
	s_cbranch_scc0 .Lc_par1
	ds_read2_b64 v[48:51], v32 offset0:0 offset1:202
	ds_read_b128 v[120:123], v33 offset:0
	ds_read2_b64 v[10:13], v34 offset0:0 offset1:202
	ds_read2_b64 v[52:55], v32 offset0:1 offset1:203
	ds_read2_b64 v[56:59], v32 offset0:2 offset1:204
	ds_read_b128 v[124:127], v33 offset:16
	ds_read2_b64 v[60:63], v32 offset0:3 offset1:205
	ds_read2_b64 v[64:67], v32 offset0:4 offset1:206
	ds_read_b128 v[128:131], v33 offset:32
	ds_read2_b64 v[68:71], v32 offset0:5 offset1:207
	s_mov_b32 s70, 0
	s_mov_b32 s71, 0
